# P11: final output stores (never re-read) marked nt
# baseline (speedup 1.0000x reference)
.LBB0_1168:
	s_add_u32 s14, s76, s6
	v_lshl_add_u64 v[4:5], s[76:77], 0, v[40:41]
	s_addc_u32 s15, s77, s7
	v_add_co_u32_e32 v72, vcc, s1, v4
	global_load_dwordx4 v[0:3], v[12:13], off
	s_nop 0
	v_addc_co_u32_e32 v73, vcc, 0, v5, vcc
	global_load_dwordx4 v[60:63], v48, s[14:15]
	global_load_dwordx4 v[64:67], v49, s[14:15]
	global_load_dwordx2 v[74:75], v[72:73], off offset:512
	global_load_dwordx2 v[76:77], v[72:73], off offset:1024
	global_load_dwordx2 v[78:79], v[72:73], off offset:1536
	global_load_dwordx2 v[80:81], v[72:73], off offset:2048
	global_load_dwordx2 v[82:83], v[72:73], off offset:2560
	global_load_dwordx2 v[84:85], v[72:73], off offset:3072
	s_ashr_i32 s16, s0, 13
	s_mul_i32 s14, s16, 0x3000
	s_ashr_i32 s15, s14, 31
	s_lshl_b64 s[14:15], s[14:15], 2
	s_add_u32 s14, s76, s14
	s_addc_u32 s15, s77, s15
	s_add_u32 s14, s14, 0xda000
	s_addc_u32 s15, s15, 0
	global_load_dwordx4 v[68:71], v50, s[14:15]
	global_load_dwordx2 v[86:87], v[72:73], off
	global_load_dwordx4 v[8:11], v52, s[14:15]
	global_load_dwordx4 v[4:7], v56, s[14:15]
	s_add_i32 s0, s0, s4
	s_add_u32 s6, s6, s8
	s_addc_u32 s7, s7, s9
	v_lshl_add_u64 v[40:41], v[40:41], 0, s[12:13]
	s_cmpk_lt_i32 s0, 0x4000
	s_waitcnt vmcnt(11)
	v_mul_f32_e32 v88, 0x3d800000, v60
	v_mul_f32_e32 v90, 0x3d800000, v61
	s_waitcnt vmcnt(10)
	v_ashrrev_i32_e32 v61, 31, v64
	v_mov_b32_e32 v60, v64
	v_mul_f32_e32 v92, 0x3d800000, v62
	v_mul_f32_e32 v94, 0x3d800000, v63
	v_ashrrev_i32_e32 v63, 31, v65
	v_mov_b32_e32 v62, v65
	v_ashrrev_i32_e32 v65, 31, v66
	v_mov_b32_e32 v64, v66
	v_ashrrev_i32_e32 v97, 31, v67
	v_mov_b32_e32 v96, v67
	v_lshlrev_b64 v[60:61], 11, v[60:61]
	s_waitcnt vmcnt(9)
	v_lshlrev_b32_e32 v98, 16, v74
	v_and_b32_e32 v99, 0xffff0000, v74
	v_lshlrev_b32_e32 v100, 16, v75
	v_and_b32_e32 v101, 0xffff0000, v75
	v_lshlrev_b64 v[62:63], 11, v[62:63]
	v_lshlrev_b64 v[66:67], 11, v[96:97]
	v_lshlrev_b64 v[64:65], 11, v[64:65]
	v_lshl_add_u64 v[74:75], v[14:15], 0, v[60:61]
	s_waitcnt vmcnt(8)
	v_lshlrev_b32_e32 v102, 16, v76
	v_and_b32_e32 v103, 0xffff0000, v76
	v_lshlrev_b32_e32 v104, 16, v77
	v_and_b32_e32 v105, 0xffff0000, v77
	s_waitcnt vmcnt(7)
	v_lshlrev_b32_e32 v106, 16, v78
	v_and_b32_e32 v107, 0xffff0000, v78
	v_lshlrev_b32_e32 v108, 16, v79
	v_and_b32_e32 v109, 0xffff0000, v79
	s_waitcnt vmcnt(6)
	v_lshlrev_b32_e32 v110, 16, v80
	v_and_b32_e32 v111, 0xffff0000, v80
	v_lshlrev_b32_e32 v112, 16, v81
	v_and_b32_e32 v113, 0xffff0000, v81
	v_lshl_add_u64 v[76:77], v[14:15], 0, v[62:63]
	v_lshl_add_u64 v[78:79], v[14:15], 0, v[64:65]
	v_lshl_add_u64 v[80:81], v[14:15], 0, v[66:67]
	global_load_dword v59, v[74:75], off
	global_load_dword v89, v[76:77], off
	global_load_dword v91, v[78:79], off
	global_load_dword v93, v[80:81], off
	v_lshl_add_u64 v[60:61], s[2:3], 0, v[60:61]
	v_lshl_add_u64 v[62:63], s[2:3], 0, v[62:63]
	v_lshl_add_u64 v[64:65], s[2:3], 0, v[64:65]
	v_lshl_add_u64 v[66:67], s[2:3], 0, v[66:67]
	v_lshl_add_u64 v[74:75], v[60:61], 0, v[16:17]
	v_lshl_add_u64 v[76:77], v[62:63], 0, v[16:17]
	v_lshl_add_u64 v[78:79], v[64:65], 0, v[16:17]
	v_lshl_add_u64 v[80:81], v[66:67], 0, v[16:17]
	v_lshl_add_u64 v[96:97], v[60:61], 0, v[18:19]
	v_lshl_add_u64 v[114:115], v[62:63], 0, v[18:19]
	v_lshl_add_u64 v[116:117], v[64:65], 0, v[18:19]
	v_lshl_add_u64 v[118:119], v[66:67], 0, v[18:19]
	v_lshl_add_u64 v[120:121], v[60:61], 0, v[20:21]
	v_lshl_add_u64 v[122:123], v[62:63], 0, v[20:21]
	v_lshl_add_u64 v[124:125], v[64:65], 0, v[20:21]
	v_lshl_add_u64 v[126:127], v[66:67], 0, v[20:21]
	v_lshl_add_u64 v[128:129], v[60:61], 0, v[22:23]
	v_lshl_add_u64 v[130:131], v[62:63], 0, v[22:23]
	v_lshl_add_u64 v[132:133], v[64:65], 0, v[22:23]
	v_lshl_add_u64 v[134:135], v[66:67], 0, v[22:23]
	v_lshl_add_u64 v[136:137], v[60:61], 0, v[24:25]
	v_lshl_add_u64 v[138:139], v[62:63], 0, v[24:25]
	v_lshl_add_u64 v[140:141], v[64:65], 0, v[24:25]
	v_lshl_add_u64 v[142:143], v[66:67], 0, v[24:25]
	v_lshl_add_u64 v[144:145], v[60:61], 0, v[26:27]
	v_lshl_add_u64 v[146:147], v[62:63], 0, v[26:27]
	v_lshl_add_u64 v[148:149], v[64:65], 0, v[26:27]
	v_lshl_add_u64 v[150:151], v[66:67], 0, v[26:27]
	v_lshl_add_u64 v[60:61], v[60:61], 0, v[28:29]
	v_lshl_add_u64 v[62:63], v[62:63], 0, v[28:29]
	v_lshl_add_u64 v[64:65], v[64:65], 0, v[28:29]
	v_lshl_add_u64 v[66:67], v[66:67], 0, v[28:29]
	global_load_dword v95, v[74:75], off
	global_load_dword v152, v[76:77], off
	global_load_dword v153, v[78:79], off
	global_load_dword v154, v[80:81], off
	global_load_dword v156, v[96:97], off
	global_load_dword v160, v[114:115], off
	global_load_dword v164, v[116:117], off
	global_load_dword v168, v[118:119], off
	global_load_dword v172, v[120:121], off
	global_load_dword v176, v[122:123], off
	global_load_dword v180, v[124:125], off
	global_load_dword v184, v[126:127], off
	global_load_dword v188, v[128:129], off
	global_load_dword v192, v[130:131], off
	global_load_dword v196, v[132:133], off
	global_load_dword v200, v[134:135], off
	global_load_dword v204, v[136:137], off
	global_load_dword v208, v[138:139], off
	global_load_dword v212, v[140:141], off
	global_load_dword v216, v[142:143], off
	global_load_dword v220, v[144:145], off
	global_load_dword v224, v[146:147], off
	global_load_dword v228, v[148:149], off
	global_load_dword v232, v[150:151], off
	global_load_dword v236, v[60:61], off
	global_load_dword v240, v[62:63], off
	global_load_dword v244, v[64:65], off
	s_nop 0
	global_load_dwordx4 v[60:63], v53, s[14:15]
	global_load_dword v250, v[66:67], off
	global_load_dwordx2 v[96:97], v[72:73], off offset:3584
	s_nop 0
	global_load_dwordx4 v[64:67], v54, s[14:15]
	global_load_dwordx4 v[72:75], v51, s[14:15]
	global_load_dwordx4 v[76:79], v55, s[14:15]
	s_waitcnt vmcnt(42)
	v_lshlrev_b32_e32 v114, 16, v82
	v_and_b32_e32 v115, 0xffff0000, v82
	v_lshlrev_b32_e32 v116, 16, v83
	v_and_b32_e32 v117, 0xffff0000, v83
	global_load_dwordx4 v[80:83], v57, s[14:15]
	s_waitcnt vmcnt(40)
	v_lshlrev_b32_e32 v120, 16, v86
	v_and_b32_e32 v121, 0xffff0000, v86
	v_lshlrev_b32_e32 v86, 16, v87
	v_and_b32_e32 v87, 0xffff0000, v87
	v_lshlrev_b32_e32 v118, 16, v84
	v_and_b32_e32 v119, 0xffff0000, v84
	v_lshlrev_b32_e32 v84, 16, v85
	v_and_b32_e32 v85, 0xffff0000, v85
	s_waitcnt vmcnt(37)
	v_cvt_pk_f32_fp8_sdwa v[124:125], v59 src0_sel:WORD_1
	v_cvt_pk_f32_fp8_e32 v[122:123], v59
	s_waitcnt vmcnt(36)
	v_cvt_pk_f32_fp8_sdwa v[128:129], v89 src0_sel:WORD_1
	s_waitcnt vmcnt(33)
	v_cvt_pk_f32_fp8_e32 v[138:139], v95
	v_cvt_pk_f32_fp8_e32 v[126:127], v89
	v_cvt_pk_f32_fp8_sdwa v[132:133], v91 src0_sel:WORD_1
	v_cvt_pk_f32_fp8_sdwa v[140:141], v95 src0_sel:WORD_1
	s_waitcnt vmcnt(32)
	v_cvt_pk_f32_fp8_e32 v[142:143], v152
	v_cvt_pk_f32_fp8_sdwa v[144:145], v152 src0_sel:WORD_1
	s_waitcnt vmcnt(31)
	v_cvt_pk_f32_fp8_e32 v[146:147], v153
	v_cvt_pk_f32_fp8_sdwa v[148:149], v153 src0_sel:WORD_1
	s_waitcnt vmcnt(30)
	v_cvt_pk_f32_fp8_e32 v[150:151], v154
	v_cvt_pk_f32_fp8_sdwa v[152:153], v154 src0_sel:WORD_1
	s_waitcnt vmcnt(29)
	v_cvt_pk_f32_fp8_e32 v[154:155], v156
	v_cvt_pk_f32_fp8_e32 v[130:131], v91
	v_cvt_pk_f32_fp8_sdwa v[136:137], v93 src0_sel:WORD_1
	v_cvt_pk_f32_fp8_sdwa v[156:157], v156 src0_sel:WORD_1
	s_waitcnt vmcnt(28)
	v_cvt_pk_f32_fp8_e32 v[158:159], v160
	s_waitcnt vmcnt(25)
	v_cvt_pk_f32_fp8_e32 v[170:171], v172
	v_cvt_pk_f32_fp8_sdwa v[172:173], v172 src0_sel:WORD_1
	s_waitcnt vmcnt(21)
	v_cvt_pk_f32_fp8_e32 v[186:187], v188
	v_cvt_pk_f32_fp8_sdwa v[188:189], v188 src0_sel:WORD_1
	s_waitcnt vmcnt(17)
	v_cvt_pk_f32_fp8_e32 v[202:203], v204
	v_cvt_pk_f32_fp8_sdwa v[204:205], v204 src0_sel:WORD_1
	s_waitcnt vmcnt(13)
	v_cvt_pk_f32_fp8_e32 v[218:219], v220
	v_cvt_pk_f32_fp8_sdwa v[220:221], v220 src0_sel:WORD_1
	s_waitcnt vmcnt(9)
	v_cvt_pk_f32_fp8_e32 v[234:235], v236
	v_cvt_pk_f32_fp8_sdwa v[236:237], v236 src0_sel:WORD_1
	v_cvt_pk_f32_fp8_e32 v[134:135], v93
	v_cvt_pk_f32_fp8_sdwa v[160:161], v160 src0_sel:WORD_1
	v_cvt_pk_f32_fp8_e32 v[162:163], v164
	v_cvt_pk_f32_fp8_e32 v[174:175], v176
	v_cvt_pk_f32_fp8_sdwa v[176:177], v176 src0_sel:WORD_1
	v_cvt_pk_f32_fp8_e32 v[190:191], v192
	v_cvt_pk_f32_fp8_sdwa v[192:193], v192 src0_sel:WORD_1
	v_cvt_pk_f32_fp8_e32 v[206:207], v208
	v_cvt_pk_f32_fp8_sdwa v[208:209], v208 src0_sel:WORD_1
	v_cvt_pk_f32_fp8_e32 v[222:223], v224
	v_cvt_pk_f32_fp8_sdwa v[224:225], v224 src0_sel:WORD_1
	s_waitcnt vmcnt(8)
	v_cvt_pk_f32_fp8_e32 v[238:239], v240
	v_cvt_pk_f32_fp8_sdwa v[240:241], v240 src0_sel:WORD_1
	v_pk_fma_f32 v[124:125], v[88:89], v[124:125], 0 op_sel_hi:[0,1,0]
	v_cvt_pk_f32_fp8_sdwa v[164:165], v164 src0_sel:WORD_1
	v_cvt_pk_f32_fp8_e32 v[166:167], v168
	v_cvt_pk_f32_fp8_e32 v[178:179], v180
	v_cvt_pk_f32_fp8_sdwa v[180:181], v180 src0_sel:WORD_1
	v_cvt_pk_f32_fp8_e32 v[194:195], v196
	v_cvt_pk_f32_fp8_sdwa v[196:197], v196 src0_sel:WORD_1
	v_cvt_pk_f32_fp8_e32 v[210:211], v212
	v_cvt_pk_f32_fp8_sdwa v[212:213], v212 src0_sel:WORD_1
	v_cvt_pk_f32_fp8_e32 v[226:227], v228
	v_cvt_pk_f32_fp8_sdwa v[228:229], v228 src0_sel:WORD_1
	s_waitcnt vmcnt(7)
	v_cvt_pk_f32_fp8_e32 v[242:243], v244
	v_cvt_pk_f32_fp8_sdwa v[244:245], v244 src0_sel:WORD_1
	v_pk_fma_f32 v[122:123], v[88:89], v[122:123], 0 op_sel_hi:[0,1,0]
	v_pk_fma_f32 v[124:125], v[90:91], v[128:129], v[124:125] op_sel_hi:[0,1,1]
	v_pk_fma_f32 v[128:129], v[88:89], v[138:139], 0 op_sel_hi:[0,1,0]
	v_cvt_pk_f32_fp8_sdwa v[168:169], v168 src0_sel:WORD_1
	v_cvt_pk_f32_fp8_e32 v[182:183], v184
	v_cvt_pk_f32_fp8_e32 v[198:199], v200
	v_cvt_pk_f32_fp8_e32 v[214:215], v216
	v_pk_fma_f32 v[122:123], v[90:91], v[126:127], v[122:123] op_sel_hi:[0,1,1]
	v_pk_fma_f32 v[126:127], v[88:89], v[140:141], 0 op_sel_hi:[0,1,0]
	v_pk_fma_f32 v[140:141], v[88:89], v[154:155], 0 op_sel_hi:[0,1,0]
	v_pk_fma_f32 v[124:125], v[92:93], v[132:133], v[124:125] op_sel_hi:[0,1,1]
	v_pk_fma_f32 v[128:129], v[90:91], v[142:143], v[128:129] op_sel_hi:[0,1,1]
	v_pk_fma_f32 v[138:139], v[88:89], v[156:157], 0 op_sel_hi:[0,1,0]
	v_pk_fma_f32 v[154:155], v[88:89], v[172:173], 0 op_sel_hi:[0,1,0]
	v_pk_fma_f32 v[156:157], v[88:89], v[170:171], 0 op_sel_hi:[0,1,0]
	v_pk_fma_f32 v[170:171], v[88:89], v[188:189], 0 op_sel_hi:[0,1,0]
	v_pk_fma_f32 v[172:173], v[88:89], v[186:187], 0 op_sel_hi:[0,1,0]
	v_pk_fma_f32 v[186:187], v[88:89], v[204:205], 0 op_sel_hi:[0,1,0]
	v_pk_fma_f32 v[188:189], v[88:89], v[202:203], 0 op_sel_hi:[0,1,0]
	v_pk_fma_f32 v[202:203], v[88:89], v[220:221], 0 op_sel_hi:[0,1,0]
	v_pk_fma_f32 v[204:205], v[88:89], v[218:219], 0 op_sel_hi:[0,1,0]
	v_pk_fma_f32 v[218:219], v[88:89], v[236:237], 0 op_sel_hi:[0,1,0]
	v_pk_fma_f32 v[88:89], v[88:89], v[234:235], 0 op_sel_hi:[0,1,0]
	v_pk_fma_f32 v[122:123], v[92:93], v[130:131], v[122:123] op_sel_hi:[0,1,1]
	v_pk_fma_f32 v[126:127], v[90:91], v[144:145], v[126:127] op_sel_hi:[0,1,1]
	v_pk_fma_f32 v[130:131], v[90:91], v[158:159], v[140:141] op_sel_hi:[0,1,1]
	v_pk_fma_f32 v[124:125], v[94:95], v[136:137], v[124:125] op_sel_hi:[0,1,1]
	v_pk_fma_f32 v[128:129], v[92:93], v[146:147], v[128:129] op_sel_hi:[0,1,1]
	v_cvt_pk_f32_fp8_sdwa v[184:185], v184 src0_sel:WORD_1
	v_cvt_pk_f32_fp8_sdwa v[200:201], v200 src0_sel:WORD_1
	v_cvt_pk_f32_fp8_sdwa v[216:217], v216 src0_sel:WORD_1
	v_cvt_pk_f32_fp8_e32 v[230:231], v232
	v_cvt_pk_f32_fp8_sdwa v[232:233], v232 src0_sel:WORD_1
	s_waitcnt vmcnt(5)
	v_cvt_pk_f32_fp8_e32 v[246:247], v250
	v_pk_fma_f32 v[132:133], v[90:91], v[160:161], v[138:139] op_sel_hi:[0,1,1]
	v_pk_fma_f32 v[138:139], v[90:91], v[174:175], v[156:157] op_sel_hi:[0,1,1]
	v_pk_fma_f32 v[140:141], v[90:91], v[176:177], v[154:155] op_sel_hi:[0,1,1]
	v_pk_fma_f32 v[142:143], v[90:91], v[190:191], v[172:173] op_sel_hi:[0,1,1]
	v_pk_fma_f32 v[144:145], v[90:91], v[192:193], v[170:171] op_sel_hi:[0,1,1]
	v_pk_fma_f32 v[154:155], v[90:91], v[206:207], v[188:189] op_sel_hi:[0,1,1]
	v_pk_fma_f32 v[156:157], v[90:91], v[208:209], v[186:187] op_sel_hi:[0,1,1]
	v_pk_fma_f32 v[158:159], v[90:91], v[222:223], v[204:205] op_sel_hi:[0,1,1]
	v_pk_fma_f32 v[160:161], v[90:91], v[224:225], v[202:203] op_sel_hi:[0,1,1]
	v_pk_fma_f32 v[88:89], v[90:91], v[238:239], v[88:89] op_sel_hi:[0,1,1]
	v_pk_fma_f32 v[90:91], v[90:91], v[240:241], v[218:219] op_sel_hi:[0,1,1]
	v_pk_fma_f32 v[122:123], v[94:95], v[134:135], v[122:123] op_sel_hi:[0,1,1]
	v_pk_fma_f32 v[126:127], v[92:93], v[148:149], v[126:127] op_sel_hi:[0,1,1]
	v_pk_fma_f32 v[130:131], v[92:93], v[162:163], v[130:131] op_sel_hi:[0,1,1]
	v_pk_fma_f32 v[70:71], v[70:71], v[124:125], v[86:87]
	v_pk_fma_f32 v[86:87], v[94:95], v[150:151], v[128:129] op_sel_hi:[0,1,1]
	v_pk_fma_f32 v[132:133], v[92:93], v[164:165], v[132:133] op_sel_hi:[0,1,1]
	v_pk_fma_f32 v[134:135], v[92:93], v[180:181], v[140:141] op_sel_hi:[0,1,1]
	v_pk_fma_f32 v[136:137], v[92:93], v[178:179], v[138:139] op_sel_hi:[0,1,1]
	v_pk_fma_f32 v[138:139], v[92:93], v[196:197], v[144:145] op_sel_hi:[0,1,1]
	v_pk_fma_f32 v[140:141], v[92:93], v[194:195], v[142:143] op_sel_hi:[0,1,1]
	v_pk_fma_f32 v[142:143], v[92:93], v[212:213], v[156:157] op_sel_hi:[0,1,1]
	v_pk_fma_f32 v[144:145], v[92:93], v[210:211], v[154:155] op_sel_hi:[0,1,1]
	v_pk_fma_f32 v[146:147], v[92:93], v[228:229], v[160:161] op_sel_hi:[0,1,1]
	v_pk_fma_f32 v[148:149], v[92:93], v[226:227], v[158:159] op_sel_hi:[0,1,1]
	v_pk_fma_f32 v[90:91], v[92:93], v[244:245], v[90:91] op_sel_hi:[0,1,1]
	v_pk_fma_f32 v[88:89], v[92:93], v[242:243], v[88:89] op_sel_hi:[0,1,1]
	v_pk_fma_f32 v[68:69], v[68:69], v[122:123], v[120:121]
	v_pk_fma_f32 v[92:93], v[94:95], v[152:153], v[126:127] op_sel_hi:[0,1,1]
	v_pk_fma_f32 v[120:121], v[94:95], v[166:167], v[130:131] op_sel_hi:[0,1,1]
	s_waitcnt vmcnt(2)
	v_pk_fma_f32 v[72:73], v[72:73], v[86:87], v[98:99]
	v_cvt_pk_f32_fp8_sdwa v[250:251], v250 src0_sel:WORD_1
	v_pk_fma_f32 v[122:123], v[94:95], v[168:169], v[132:133] op_sel_hi:[0,1,1]
	v_pk_fma_f32 v[124:125], v[94:95], v[182:183], v[136:137] op_sel_hi:[0,1,1]
	v_pk_fma_f32 v[128:129], v[94:95], v[198:199], v[140:141] op_sel_hi:[0,1,1]
	v_pk_fma_f32 v[132:133], v[94:95], v[214:215], v[144:145] op_sel_hi:[0,1,1]
	v_mul_f32_e32 v59, v69, v69
	v_pk_fma_f32 v[74:75], v[74:75], v[92:93], v[100:101]
	v_pk_fma_f32 v[8:9], v[8:9], v[120:121], v[102:103]
	v_mul_f32_e32 v100, v73, v73
	v_pk_fma_f32 v[60:61], v[60:61], v[124:125], v[106:107]
	v_pk_fma_f32 v[64:65], v[64:65], v[128:129], v[110:111]
	s_waitcnt vmcnt(1)
	v_pk_fma_f32 v[76:77], v[76:77], v[132:133], v[114:115]
	v_fmac_f32_e32 v59, v68, v68
	v_mul_f32_e32 v101, v9, v9
	v_fmac_f32_e32 v100, v72, v72
	v_lshlrev_b32_e32 v248, 16, v96
	v_and_b32_e32 v249, 0xffff0000, v96
	v_pk_fma_f32 v[126:127], v[94:95], v[184:185], v[134:135] op_sel_hi:[0,1,1]
	v_pk_fma_f32 v[130:131], v[94:95], v[200:201], v[138:139] op_sel_hi:[0,1,1]
	v_pk_fma_f32 v[134:135], v[94:95], v[216:217], v[142:143] op_sel_hi:[0,1,1]
	v_pk_fma_f32 v[136:137], v[94:95], v[230:231], v[148:149] op_sel_hi:[0,1,1]
	v_pk_fma_f32 v[138:139], v[94:95], v[232:233], v[146:147] op_sel_hi:[0,1,1]
	v_pk_fma_f32 v[88:89], v[94:95], v[246:247], v[88:89] op_sel_hi:[0,1,1]
	v_pk_fma_f32 v[10:11], v[10:11], v[122:123], v[104:105]
	v_mul_f32_e32 v102, v61, v61
	v_mov_b32_e32 v86, v65
	v_mov_b32_e32 v87, v77
	v_fmac_f32_e32 v59, v70, v70
	v_fmac_f32_e32 v101, v8, v8
	v_fmac_f32_e32 v100, v74, v74
	v_pk_fma_f32 v[62:63], v[62:63], v[126:127], v[108:109]
	v_pk_fma_f32 v[66:67], v[66:67], v[130:131], v[112:113]
	v_pk_fma_f32 v[78:79], v[78:79], v[134:135], v[116:117]
	v_pk_fma_f32 v[6:7], v[6:7], v[138:139], v[84:85]
	v_pk_fma_f32 v[4:5], v[4:5], v[136:137], v[118:119]
	s_waitcnt vmcnt(0)
	v_pk_fma_f32 v[80:81], v[80:81], v[88:89], v[248:249]
	v_mov_b32_e32 v84, v64
	v_mov_b32_e32 v85, v76
	v_fmac_f32_e32 v102, v60, v60
	v_pk_mul_f32 v[86:87], v[86:87], v[86:87]
	v_fmac_f32_e32 v59, v71, v71
	v_fmac_f32_e32 v101, v10, v10
	v_fmac_f32_e32 v100, v75, v75
	v_lshlrev_b32_e32 v96, 16, v97
	v_and_b32_e32 v97, 0xffff0000, v97
	v_pk_fma_f32 v[90:91], v[94:95], v[250:251], v[90:91] op_sel_hi:[0,1,1]
	v_mov_b32_e32 v88, v66
	v_mov_b32_e32 v89, v78
	v_mov_b32_e32 v94, v5
	v_mov_b32_e32 v95, v81
	v_fmac_f32_e32 v102, v62, v62
	v_pk_fma_f32 v[84:85], v[84:85], v[84:85], v[86:87]
	v_fmac_f32_e32 v101, v11, v11
	v_add_f32_e32 v59, v59, v100
	v_pk_fma_f32 v[82:83], v[82:83], v[90:91], v[96:97]
	v_mov_b32_e32 v90, v67
	v_mov_b32_e32 v91, v79
	v_mov_b32_e32 v92, v4
	v_mov_b32_e32 v93, v80
	v_pk_mul_f32 v[94:95], v[94:95], v[94:95]
	v_fmac_f32_e32 v102, v63, v63
	v_pk_fma_f32 v[84:85], v[88:89], v[88:89], v[84:85]
	v_add_f32_e32 v59, v59, v101
	v_mov_b32_e32 v96, v6
	v_mov_b32_e32 v97, v82
	v_pk_fma_f32 v[86:87], v[92:93], v[92:93], v[94:95]
	v_pk_fma_f32 v[84:85], v[90:91], v[90:91], v[84:85]
	v_add_f32_e32 v59, v59, v102
	v_mov_b32_e32 v98, v7
	v_mov_b32_e32 v99, v83
	v_pk_fma_f32 v[86:87], v[96:97], v[96:97], v[86:87]
	v_add_f32_e32 v59, v59, v84
	v_pk_fma_f32 v[86:87], v[98:99], v[98:99], v[86:87]
	v_add_f32_e32 v59, v59, v85
	v_add_f32_e32 v59, v59, v86
	v_add_f32_e32 v59, v59, v87
	ds_bpermute_b32 v84, v42, v59
	s_waitcnt lgkmcnt(0)
	v_add_f32_e32 v59, v59, v84
	ds_bpermute_b32 v84, v43, v59
	s_waitcnt lgkmcnt(0)
	v_add_f32_e32 v59, v59, v84
	s_nop 1
	v_mov_b32_dpp v84, v59 row_ror:8 row_mask:0xf bank_mask:0xf
	s_waitcnt lgkmcnt(0)
	v_add_f32_e32 v59, v59, v84
	s_nop 1
	v_mov_b32_dpp v84, v59 row_ror:4 row_mask:0xf bank_mask:0xf
	s_waitcnt lgkmcnt(0)
	v_add_f32_e32 v59, v59, v84
	s_nop 1
	v_mov_b32_dpp v84, v59 quad_perm:[2,3,0,1] row_mask:0xf bank_mask:0xf
	s_waitcnt lgkmcnt(0)
	v_add_f32_e32 v59, v59, v84
	s_nop 1
	v_mov_b32_dpp v84, v59 quad_perm:[1,0,3,2] row_mask:0xf bank_mask:0xf
	s_waitcnt lgkmcnt(0)
	v_add_f32_e32 v59, v59, v84
	v_fmamk_f32 v59, v59, 0x3a000000, v58
	v_mul_f32_e32 v84, 0x4b800000, v59
	v_cmp_gt_f32_e32 vcc, s5, v59
	s_nop 1
	v_cndmask_b32_e32 v59, v59, v84, vcc
	v_rsq_f32_e32 v59, v59
	s_nop 0
	v_mul_f32_e32 v84, 0x45800000, v59
	v_cndmask_b32_e32 v84, v59, v84, vcc
	v_pk_mul_f32 v[68:69], v[68:69], v[84:85] op_sel_hi:[1,0]
	v_pk_mul_f32 v[70:71], v[70:71], v[84:85] op_sel_hi:[1,0]
	v_pk_mul_f32 v[0:1], v[0:1], v[68:69]
	v_pk_mul_f32 v[2:3], v[2:3], v[70:71]
	global_store_dwordx4 v[38:39], v[0:3], off offset:-4096 nt
	global_load_dwordx4 v[0:3], v[12:13], off offset:1024
	v_pk_mul_f32 v[68:69], v[74:75], v[84:85] op_sel_hi:[1,0]
	v_pk_mul_f32 v[70:71], v[72:73], v[84:85] op_sel_hi:[1,0]
	v_pk_mul_f32 v[10:11], v[10:11], v[84:85] op_sel_hi:[1,0]
	v_pk_mul_f32 v[8:9], v[8:9], v[84:85] op_sel_hi:[1,0]
	v_pk_mul_f32 v[6:7], v[6:7], v[84:85] op_sel_hi:[1,0]
	v_pk_mul_f32 v[4:5], v[4:5], v[84:85] op_sel_hi:[1,0]
	s_waitcnt vmcnt(0)
	v_pk_mul_f32 v[0:1], v[0:1], v[70:71]
	v_pk_mul_f32 v[2:3], v[2:3], v[68:69]
	global_store_dwordx4 v[38:39], v[0:3], off offset:-3072 nt
	global_load_dwordx4 v[0:3], v[12:13], off offset:2048
	s_waitcnt vmcnt(0)
	v_pk_mul_f32 v[0:1], v[0:1], v[8:9]
	v_pk_mul_f32 v[2:3], v[2:3], v[10:11]
	global_store_dwordx4 v[38:39], v[0:3], off offset:-2048 nt
	global_load_dwordx4 v[0:3], v[12:13], off offset:3072
	v_pk_mul_f32 v[8:9], v[62:63], v[84:85] op_sel_hi:[1,0]
	v_pk_mul_f32 v[10:11], v[60:61], v[84:85] op_sel_hi:[1,0]
	s_waitcnt vmcnt(0)
	v_pk_mul_f32 v[2:3], v[2:3], v[8:9]
	v_pk_mul_f32 v[0:1], v[0:1], v[10:11]
	global_store_dwordx4 v[38:39], v[0:3], off offset:-1024 nt
	global_load_dwordx4 v[0:3], v[30:31], off
	v_pk_mul_f32 v[8:9], v[66:67], v[84:85] op_sel_hi:[1,0]
	v_pk_mul_f32 v[10:11], v[64:65], v[84:85] op_sel_hi:[1,0]
	s_waitcnt vmcnt(0)
	v_pk_mul_f32 v[2:3], v[2:3], v[8:9]
	v_pk_mul_f32 v[0:1], v[0:1], v[10:11]
	global_store_dwordx4 v[38:39], v[0:3], off nt
	global_load_dwordx4 v[0:3], v[32:33], off
	v_pk_mul_f32 v[8:9], v[78:79], v[84:85] op_sel_hi:[1,0]
	v_pk_mul_f32 v[10:11], v[76:77], v[84:85] op_sel_hi:[1,0]
	s_waitcnt vmcnt(0)
	v_pk_mul_f32 v[2:3], v[2:3], v[8:9]
	v_pk_mul_f32 v[0:1], v[0:1], v[10:11]
	global_store_dwordx4 v[38:39], v[0:3], off offset:1024 nt
	global_load_dwordx4 v[0:3], v[34:35], off
	s_waitcnt vmcnt(0)
	v_pk_mul_f32 v[0:1], v[0:1], v[4:5]
	v_pk_mul_f32 v[2:3], v[2:3], v[6:7]
	global_store_dwordx4 v[38:39], v[0:3], off offset:2048 nt
	global_load_dwordx4 v[0:3], v[36:37], off
	v_pk_mul_f32 v[4:5], v[82:83], v[84:85] op_sel_hi:[1,0]
	v_pk_mul_f32 v[6:7], v[80:81], v[84:85] op_sel_hi:[1,0]
	s_waitcnt vmcnt(0)
	v_pk_mul_f32 v[2:3], v[2:3], v[4:5]
	v_pk_mul_f32 v[0:1], v[0:1], v[6:7]
	global_store_dwordx4 v[38:39], v[0:3], off offset:3072 nt
	v_lshl_add_u64 v[38:39], v[38:39], 0, s[10:11]
	s_cbranch_scc1 .LBB0_1168
